# fp8 MoE GEMM K-loops: extra priority windows (setprio 0 then 1) after every 4 MFMAs instead of every 8
# speedup vs baseline: 1.0059x; 1.0059x over previous
; #define PG8_STAGE(bufoff, gbase, voff) do { _Pragma("unroll") for (int _i = 0; _i < 2; ++_i) \
;         __builtin_amdgcn_global_load_lds((const unsigned*)((const char*)(gbase) + (voff)[_i]), (PG8_LAS unsigned*)(lds + (bufoff) + ldsw + _i * 8192), 16, 0, 0); } while (0)
; #define PG8_WAIT_V(n) asm volatile("s_waitcnt vmcnt(" #n ")" ::: "memory")
; #define PG8_WAIT_L(n) asm volatile("s_waitcnt lgkmcnt(" #n ")" ::: "memory")
; #define PG8_BAR __builtin_amdgcn_s_barrier()
; #define PG8_SCHED __builtin_amdgcn_sched_barrier(0)
; template <class Epi, class Sched, bool ALIGN_EPI = false, bool SP2 = false, bool FP8 = false, bool I8 = false>
; __device__ __forceinline__ void gemm_phase(PG8_LAS unsigned char* lds, const Gemm g, const Sched& S, const Epi& E) {
;     ...
;             PG8_LDA(At, 0, 1); PG8_STAGE(PG8_SB(0, 0), b2, voffB); PG8_STAGE(PG8_SB(0, 1), b2 + hstep, voffB); PG8_STAGE(PG8_SA(0, 0), a2, voffA);
;             PG8_WAIT_V(8); PG8_WAIT_L(0); PG8_BAR; PG8_MMA(1, 0, At, B0); PG8_MMA(1, 1, At, B1); PG8_BAR; PG8_SCHED;
;             PG8_LDB(B0, 1, 0); PG8_LDB(B1, 1, 1); PG8_SCHED; PG8_LDA(At, 1, 0); PG8_STAGE(PG8_SA(0, 1), a2 + hstepA, voffA1);
;             PG8_WAIT_V(8); PG8_WAIT_L(0); PG8_BAR; PG8_MMA(0, 0, At, B0); PG8_MMA(0, 1, At, B1); PG8_BAR; PG8_SCHED;
.LBB0_1917:
	v_lshl_add_u64 v[182:183], v[180:181], 0, s[2:3]
	s_add_u32 s61, s90, s2
	v_cndmask_b32_e64 v183, v183, v179, s[10:11]
	v_cndmask_b32_e64 v182, v182, v178, s[10:11]
	s_mov_b32 m0, s45
	s_addc_u32 s62, s91, s3
	v_lshl_add_u64 v[186:187], v[182:183], 0, v[166:167]
	s_add_u32 s61, s61, 0x34200100
	ds_read_b128 v[202:205], v198 offset:16384
	ds_read_b128 v[206:209], v198 offset:17408
	ds_read_b128 v[210:213], v198 offset:18432
	ds_read_b128 v[214:217], v198 offset:19456
	ds_read_b128 v[218:221], v198 offset:20480
	ds_read_b128 v[222:225], v198 offset:21504
	ds_read_b128 v[226:229], v198 offset:22528
	ds_read_b128 v[230:233], v198 offset:23552
	global_load_lds_dwordx4 v[186:187], off
	v_lshl_add_u64 v[184:185], v[182:183], 0, v[168:169]
	s_mov_b32 m0, s46
	v_lshl_add_u64 v[188:189], v[182:183], 0, s[18:19]
	s_addc_u32 s62, s62, 0
	global_load_lds_dwordx4 v[184:185], off
	v_lshl_add_u64 v[190:191], v[188:189], 0, v[166:167]
	s_mov_b32 m0, s47
	s_and_b64 s[10:11], s[10:11], exec
	global_load_lds_dwordx4 v[190:191], off
	v_lshl_add_u64 v[188:189], v[188:189], 0, v[168:169]
	s_mov_b32 m0, s48
	s_cselect_b32 s11, s15, s62
	s_cselect_b32 s10, s14, s61
	global_load_lds_dwordx4 v[188:189], off
	s_mov_b32 m0, s1
	v_mov_b32_e32 v173, v171
	global_load_lds_dwordx4 v172, s[10:11]
	s_mov_b32 m0, s49
	v_mov_b32_e32 v175, v171
	global_load_lds_dwordx4 v174, s[10:11]
	s_waitcnt vmcnt(8)
	s_waitcnt lgkmcnt(0)
	v_lshl_add_u64 v[190:191], s[10:11], 0, v[172:173]
	v_lshl_add_u64 v[188:189], s[10:11], 0, v[174:175]
	s_barrier
	s_setprio 1
	s_waitcnt lgkmcnt(0)
	v_mfma_scale_f32_16x16x128_f8f6f4 v[94:97], v[18:25], v[202:209], v[94:97], v197, v197 op_sel_hi:[0,0,0]
	v_mfma_scale_f32_16x16x128_f8f6f4 v[90:93], v[26:33], v[202:209], v[90:93], v197, v197 op_sel_hi:[0,0,0]
	v_mfma_scale_f32_16x16x128_f8f6f4 v[86:89], v[18:25], v[210:217], v[86:89], v197, v197 op_sel_hi:[0,0,0]
	v_mfma_scale_f32_16x16x128_f8f6f4 v[82:85], v[26:33], v[210:217], v[82:85], v197, v197 op_sel_hi:[0,0,0]
	s_setprio 0
	s_setprio 1
	v_mfma_scale_f32_16x16x128_f8f6f4 v[78:81], v[18:25], v[218:225], v[78:81], v197, v197 op_sel_hi:[0,0,0]
	v_mfma_scale_f32_16x16x128_f8f6f4 v[74:77], v[26:33], v[218:225], v[74:77], v197, v197 op_sel_hi:[0,0,0]
	v_mfma_scale_f32_16x16x128_f8f6f4 v[70:73], v[18:25], v[226:233], v[70:73], v197, v197 op_sel_hi:[0,0,0]
	v_mfma_scale_f32_16x16x128_f8f6f4 v[66:69], v[26:33], v[226:233], v[66:69], v197, v197 op_sel_hi:[0,0,0]
	s_setprio 0
	s_setprio 1
	v_mfma_scale_f32_16x16x128_f8f6f4 v[62:65], v[2:9], v[202:209], v[62:65], v197, v197 op_sel_hi:[0,0,0]
	v_mfma_scale_f32_16x16x128_f8f6f4 v[58:61], v[10:17], v[202:209], v[58:61], v197, v197 op_sel_hi:[0,0,0]
	v_mfma_scale_f32_16x16x128_f8f6f4 v[54:57], v[2:9], v[210:217], v[54:57], v197, v197 op_sel_hi:[0,0,0]
	v_mfma_scale_f32_16x16x128_f8f6f4 v[50:53], v[10:17], v[210:217], v[50:53], v197, v197 op_sel_hi:[0,0,0]
	s_setprio 0
	s_setprio 1
	v_mfma_scale_f32_16x16x128_f8f6f4 v[46:49], v[2:9], v[218:225], v[46:49], v197, v197 op_sel_hi:[0,0,0]
	v_mfma_scale_f32_16x16x128_f8f6f4 v[42:45], v[10:17], v[218:225], v[42:45], v197, v197 op_sel_hi:[0,0,0]
	v_mfma_scale_f32_16x16x128_f8f6f4 v[38:41], v[2:9], v[226:233], v[38:41], v197, v197 op_sel_hi:[0,0,0]
	v_mfma_scale_f32_16x16x128_f8f6f4 v[34:37], v[10:17], v[226:233], v[34:37], v197, v197 op_sel_hi:[0,0,0]
	s_setprio 0
	s_barrier
	s_add_i32 s61, 0, 0x18000
	s_add_i32 s62, 0, 0x1c000
	v_add_u32_e32 v14, s61, v195
	v_add_u32_e32 v30, s62, v195
	ds_read_b128 v[2:5], v14
	ds_read_b128 v[6:9], v14 offset:1024
	ds_read_b128 v[10:13], v14 offset:2048
	ds_read_b128 v[14:17], v14 offset:3072
	ds_read_b128 v[18:21], v30
	ds_read_b128 v[22:25], v30 offset:1024
	ds_read_b128 v[26:29], v30 offset:2048
	ds_read_b128 v[30:33], v30 offset:3072
	s_mov_b32 m0, s50
	v_lshl_add_u64 v[234:235], s[10:11], 0, v[170:171]
	ds_read_b128 v[202:205], v198 offset:32768
	ds_read_b128 v[206:209], v198 offset:33792
	ds_read_b128 v[210:213], v198 offset:34816
	ds_read_b128 v[214:217], v198 offset:35840
	ds_read_b128 v[218:221], v198 offset:36864
	ds_read_b128 v[222:225], v198 offset:37888
	ds_read_b128 v[226:229], v198 offset:38912
	ds_read_b128 v[230:233], v198 offset:39936
	global_load_lds_dwordx4 v[234:235], off
	v_lshl_add_u64 v[234:235], s[10:11], 0, v[176:177]
	s_mov_b32 m0, s51
	s_nop 0
	global_load_lds_dwordx4 v[234:235], off
	s_waitcnt vmcnt(8)
	s_waitcnt lgkmcnt(0)
	s_barrier
	s_setprio 1
	s_waitcnt lgkmcnt(0)
	v_mfma_scale_f32_16x16x128_f8f6f4 v[158:161], v[2:9], v[202:209], v[158:161], v197, v197 op_sel_hi:[0,0,0]
	v_mfma_scale_f32_16x16x128_f8f6f4 v[154:157], v[10:17], v[202:209], v[154:157], v197, v197 op_sel_hi:[0,0,0]
	v_mfma_scale_f32_16x16x128_f8f6f4 v[150:153], v[2:9], v[210:217], v[150:153], v197, v197 op_sel_hi:[0,0,0]
	v_mfma_scale_f32_16x16x128_f8f6f4 v[146:149], v[10:17], v[210:217], v[146:149], v197, v197 op_sel_hi:[0,0,0]
	s_setprio 0
	s_setprio 1
	v_mfma_scale_f32_16x16x128_f8f6f4 v[142:145], v[2:9], v[218:225], v[142:145], v197, v197 op_sel_hi:[0,0,0]
	v_mfma_scale_f32_16x16x128_f8f6f4 v[138:141], v[10:17], v[218:225], v[138:141], v197, v197 op_sel_hi:[0,0,0]
	v_mfma_scale_f32_16x16x128_f8f6f4 v[134:137], v[2:9], v[226:233], v[134:137], v197, v197 op_sel_hi:[0,0,0]
	v_mfma_scale_f32_16x16x128_f8f6f4 v[130:133], v[10:17], v[226:233], v[130:133], v197, v197 op_sel_hi:[0,0,0]
	s_setprio 0
	s_setprio 1
	v_mfma_scale_f32_16x16x128_f8f6f4 v[126:129], v[18:25], v[202:209], v[126:129], v197, v197 op_sel_hi:[0,0,0]
	v_mfma_scale_f32_16x16x128_f8f6f4 v[122:125], v[26:33], v[202:209], v[122:125], v197, v197 op_sel_hi:[0,0,0]
	v_mfma_scale_f32_16x16x128_f8f6f4 v[118:121], v[18:25], v[210:217], v[118:121], v197, v197 op_sel_hi:[0,0,0]
	v_mfma_scale_f32_16x16x128_f8f6f4 v[114:117], v[26:33], v[210:217], v[114:117], v197, v197 op_sel_hi:[0,0,0]
	s_setprio 0
	s_setprio 1
	v_mfma_scale_f32_16x16x128_f8f6f4 v[110:113], v[18:25], v[218:225], v[110:113], v197, v197 op_sel_hi:[0,0,0]
	v_mfma_scale_f32_16x16x128_f8f6f4 v[106:109], v[26:33], v[218:225], v[106:109], v197, v197 op_sel_hi:[0,0,0]
	v_mfma_scale_f32_16x16x128_f8f6f4 v[102:105], v[18:25], v[226:233], v[102:105], v197, v197 op_sel_hi:[0,0,0]
	v_mfma_scale_f32_16x16x128_f8f6f4 v[98:101], v[26:33], v[226:233], v[98:101], v197, v197 op_sel_hi:[0,0,0]
	s_setprio 0
	s_barrier
; #define PG8_ROWS(_u) do { _Pragma("unroll") for (int _i = 0; _i < 2; ++_i) { voffA[_i] = S.row_off((_u), rselA[_i]) + cselA[_i]; voffA1[_i] = S.row_off((_u), HALF + rselA[_i]) + cselA[_i]; } } while (0)
; #define PG8_STAGE(bufoff, gbase, voff) do { _Pragma("unroll") for (int _i = 0; _i < 2; ++_i) \
;         __builtin_amdgcn_global_load_lds((const unsigned*)((const char*)(gbase) + (voff)[_i]), (PG8_LAS unsigned*)(lds + (bufoff) + ldsw + _i * 8192), 16, 0, 0); } while (0)
; #define PG8_WAIT_V(n) asm volatile("s_waitcnt vmcnt(" #n ")" ::: "memory")
; #define PG8_WAIT_L(n) asm volatile("s_waitcnt lgkmcnt(" #n ")" ::: "memory")
; #define PG8_BAR __builtin_amdgcn_s_barrier()
; #define PG8_SCHED __builtin_amdgcn_sched_barrier(0)
; template <class Epi, class Sched, bool ALIGN_EPI = false, bool SP2 = false, bool FP8 = false, bool I8 = false>
; __device__ __forceinline__ void gemm_phase(PG8_LAS unsigned char* lds, const Gemm g, const Sched& S, const Epi& E) {
;     ...
;             PG8_LDB(B0, 0, 0); PG8_LDB(B1, 0, 1); PG8_SCHED; PG8_LDA(At, 0, 0); PG8_STAGE(PG8_SA(1, 1), a1 + hstepA, voffA1);
;             PG8_WAIT_V(8); PG8_WAIT_L(0); PG8_BAR; PG8_MMA(0, 0, At, B0); PG8_MMA(0, 1, At, B1); PG8_BAR; PG8_SCHED;
;             if constexpr (Sched::GATHER) { if (last && has_next) PG8_ROWS(ui + 1); }
;     ...
;             PG8_LDA(At, 1, 1); PG8_STAGE(PG8_SB(1, 0), b3, voffB); PG8_STAGE(PG8_SB(1, 1), b3 + hstep, voffB); PG8_STAGE(PG8_SA(1, 0), a3, voffA);
;             PG8_WAIT_V(8); PG8_WAIT_L(0); PG8_BAR; PG8_MMA(1, 0, At, B0); PG8_MMA(1, 1, At, B1); PG8_BAR; PG8_SCHED;
	s_add_i32 s10, s61, s44
	v_lshl_add_u64 v[186:187], v[186:187], 0, s[24:25]
	s_mov_b32 m0, s10
	ds_read_b128 v[202:205], v198 offset:49152
	ds_read_b128 v[206:209], v198 offset:50176
	ds_read_b128 v[210:213], v198 offset:51200
	ds_read_b128 v[214:217], v198 offset:52224
	ds_read_b128 v[218:221], v198 offset:53248
	ds_read_b128 v[222:225], v198 offset:54272
	ds_read_b128 v[226:229], v198 offset:55296
	ds_read_b128 v[230:233], v198 offset:56320
	global_load_lds_dwordx4 v[186:187], off
	v_lshl_add_u64 v[184:185], v[184:185], 0, s[24:25]
	s_add_i32 m0, s10, 0x2000
	v_lshl_add_u64 v[182:183], v[182:183], 0, s[28:29]
	s_add_i32 s10, s62, s44
	global_load_lds_dwordx4 v[184:185], off
	v_lshl_add_u64 v[184:185], v[182:183], 0, v[166:167]
	s_mov_b32 m0, s10
	v_lshl_add_u64 v[182:183], v[182:183], 0, v[168:169]
	global_load_lds_dwordx4 v[184:185], off
	s_add_i32 m0, s10, 0x2000
	s_nop 0
	global_load_lds_dwordx4 v[182:183], off
	v_lshl_add_u64 v[182:183], v[190:191], 0, s[24:25]
	s_mov_b32 m0, s53
	s_nop 0
	global_load_lds_dwordx4 v[182:183], off
	v_lshl_add_u64 v[182:183], v[188:189], 0, s[24:25]
	s_mov_b32 m0, s54
	s_nop 0
	global_load_lds_dwordx4 v[182:183], off
	s_waitcnt vmcnt(8)
	s_waitcnt lgkmcnt(0)
	s_barrier
	s_setprio 1
	s_waitcnt lgkmcnt(0)
	v_mfma_scale_f32_16x16x128_f8f6f4 v[94:97], v[2:9], v[202:209], v[94:97], v197, v197 op_sel_hi:[0,0,0]
	v_mfma_scale_f32_16x16x128_f8f6f4 v[90:93], v[10:17], v[202:209], v[90:93], v197, v197 op_sel_hi:[0,0,0]
	v_mfma_scale_f32_16x16x128_f8f6f4 v[86:89], v[2:9], v[210:217], v[86:89], v197, v197 op_sel_hi:[0,0,0]
	v_mfma_scale_f32_16x16x128_f8f6f4 v[82:85], v[10:17], v[210:217], v[82:85], v197, v197 op_sel_hi:[0,0,0]
	s_setprio 0
	s_setprio 1
	v_mfma_scale_f32_16x16x128_f8f6f4 v[78:81], v[2:9], v[218:225], v[78:81], v197, v197 op_sel_hi:[0,0,0]
	v_mfma_scale_f32_16x16x128_f8f6f4 v[74:77], v[10:17], v[218:225], v[74:77], v197, v197 op_sel_hi:[0,0,0]
	v_mfma_scale_f32_16x16x128_f8f6f4 v[70:73], v[2:9], v[226:233], v[70:73], v197, v197 op_sel_hi:[0,0,0]
	v_mfma_scale_f32_16x16x128_f8f6f4 v[66:69], v[10:17], v[226:233], v[66:69], v197, v197 op_sel_hi:[0,0,0]
	s_setprio 0
	s_setprio 1
	v_mfma_scale_f32_16x16x128_f8f6f4 v[62:65], v[18:25], v[202:209], v[62:65], v197, v197 op_sel_hi:[0,0,0]
	v_mfma_scale_f32_16x16x128_f8f6f4 v[58:61], v[26:33], v[202:209], v[58:61], v197, v197 op_sel_hi:[0,0,0]
	v_mfma_scale_f32_16x16x128_f8f6f4 v[54:57], v[18:25], v[210:217], v[54:57], v197, v197 op_sel_hi:[0,0,0]
	v_mfma_scale_f32_16x16x128_f8f6f4 v[50:53], v[26:33], v[210:217], v[50:53], v197, v197 op_sel_hi:[0,0,0]
	s_setprio 0
	s_setprio 1
	v_mfma_scale_f32_16x16x128_f8f6f4 v[46:49], v[18:25], v[218:225], v[46:49], v197, v197 op_sel_hi:[0,0,0]
	v_mfma_scale_f32_16x16x128_f8f6f4 v[42:45], v[26:33], v[218:225], v[42:45], v197, v197 op_sel_hi:[0,0,0]
	v_mfma_scale_f32_16x16x128_f8f6f4 v[38:41], v[18:25], v[226:233], v[38:41], v197, v197 op_sel_hi:[0,0,0]
	v_mfma_scale_f32_16x16x128_f8f6f4 v[34:37], v[26:33], v[226:233], v[34:37], v197, v197 op_sel_hi:[0,0,0]
	s_setprio 0
	s_barrier
	s_add_i32 s41, s41, 2
	s_add_u32 s2, s2, 0x100
	s_addc_u32 s3, s3, 0
	s_cmp_gt_u32 s41, 13
	s_cbranch_scc1 .LBB0_1920
.LBB0_1918:
	v_add_u32_e32 v2, 0, v195
	v_add_u32_e32 v3, 0x10000, v2
	v_add_u32_e32 v14, 0x14000, v2
	ds_read_b128 v[18:21], v3
	ds_read_b128 v[22:25], v3 offset:1024
	ds_read_b128 v[26:29], v3 offset:2048
	ds_read_b128 v[30:33], v3 offset:3072
	ds_read_b128 v[2:5], v14
	ds_read_b128 v[6:9], v14 offset:1024
	ds_read_b128 v[10:13], v14 offset:2048
	ds_read_b128 v[14:17], v14 offset:3072
	s_cmp_eq_u32 s41, 12
	s_cselect_b64 s[10:11], -1, 0
	s_add_u32 s62, s90, s2
	s_addc_u32 s63, s91, s3
	v_lshl_add_u64 v[190:191], s[62:63], 0, v[170:171]
	v_lshl_add_u64 v[190:191], v[190:191], 0, s[26:27]
	s_add_i32 m0, s1, 0xc000
	v_mov_b32_e32 v177, v171
	ds_read_b128 v[182:185], v198
	ds_read_b128 v[186:189], v198 offset:1024
	ds_read_b128 v[202:205], v198 offset:2048
	ds_read_b128 v[206:209], v198 offset:3072
	ds_read_b128 v[210:213], v198 offset:4096
	ds_read_b128 v[214:217], v198 offset:5120
	ds_read_b128 v[218:221], v198 offset:6144
	ds_read_b128 v[222:225], v198 offset:7168
	global_load_lds_dwordx4 v[190:191], off
	v_lshl_add_u64 v[190:191], s[62:63], 0, v[176:177]
	v_lshl_add_u64 v[190:191], v[190:191], 0, s[26:27]
	s_add_i32 m0, s1, 0xe000
	s_nop 0
	global_load_lds_dwordx4 v[190:191], off
	s_waitcnt vmcnt(8)
	s_waitcnt lgkmcnt(0)
	s_barrier
	s_setprio 1
	s_waitcnt lgkmcnt(0)
	v_mfma_scale_f32_16x16x128_f8f6f4 v[158:161], v[18:25], v[182:189], v[158:161], v197, v197 op_sel_hi:[0,0,0]
	v_mfma_scale_f32_16x16x128_f8f6f4 v[154:157], v[26:33], v[182:189], v[154:157], v197, v197 op_sel_hi:[0,0,0]
	v_mfma_scale_f32_16x16x128_f8f6f4 v[150:153], v[18:25], v[202:209], v[150:153], v197, v197 op_sel_hi:[0,0,0]
	v_mfma_scale_f32_16x16x128_f8f6f4 v[146:149], v[26:33], v[202:209], v[146:149], v197, v197 op_sel_hi:[0,0,0]
	s_setprio 0
	s_setprio 1
	v_mfma_scale_f32_16x16x128_f8f6f4 v[142:145], v[18:25], v[210:217], v[142:145], v197, v197 op_sel_hi:[0,0,0]
	v_mfma_scale_f32_16x16x128_f8f6f4 v[138:141], v[26:33], v[210:217], v[138:141], v197, v197 op_sel_hi:[0,0,0]
	v_mfma_scale_f32_16x16x128_f8f6f4 v[134:137], v[18:25], v[218:225], v[134:137], v197, v197 op_sel_hi:[0,0,0]
	v_mfma_scale_f32_16x16x128_f8f6f4 v[130:133], v[26:33], v[218:225], v[130:133], v197, v197 op_sel_hi:[0,0,0]
	s_setprio 0
	s_setprio 1
	v_mfma_scale_f32_16x16x128_f8f6f4 v[126:129], v[2:9], v[182:189], v[126:129], v197, v197 op_sel_hi:[0,0,0]
	v_mfma_scale_f32_16x16x128_f8f6f4 v[122:125], v[10:17], v[182:189], v[122:125], v197, v197 op_sel_hi:[0,0,0]
	v_mfma_scale_f32_16x16x128_f8f6f4 v[118:121], v[2:9], v[202:209], v[118:121], v197, v197 op_sel_hi:[0,0,0]
	v_mfma_scale_f32_16x16x128_f8f6f4 v[114:117], v[10:17], v[202:209], v[114:117], v197, v197 op_sel_hi:[0,0,0]
	s_setprio 0
	s_setprio 1
	v_mfma_scale_f32_16x16x128_f8f6f4 v[110:113], v[2:9], v[210:217], v[110:113], v197, v197 op_sel_hi:[0,0,0]
	v_mfma_scale_f32_16x16x128_f8f6f4 v[106:109], v[10:17], v[210:217], v[106:109], v197, v197 op_sel_hi:[0,0,0]
	v_mfma_scale_f32_16x16x128_f8f6f4 v[102:105], v[2:9], v[218:225], v[102:105], v197, v197 op_sel_hi:[0,0,0]
	v_mfma_scale_f32_16x16x128_f8f6f4 v[98:101], v[10:17], v[218:225], v[98:101], v197, v197 op_sel_hi:[0,0,0]
	s_and_b64 s[62:63], s[8:9], s[10:11]
	s_setprio 0
	s_barrier
	s_andn2_b64 vcc, exec, s[62:63]
	s_cbranch_vccnz .LBB0_1917
	ds_read2st64_b32 v[172:173], v200 offset1:2
	ds_read2st64_b32 v[174:175], v201 offset1:2
	v_mov_b32_e32 v177, v171
	s_waitcnt lgkmcnt(0)
	v_add_u32_e32 v172, v172, v1
	v_add_u32_e32 v170, v173, v1
	v_add_u32_e32 v174, v174, v1
	v_add_u32_e32 v176, v175, v1
	s_branch .LBB0_1917

; #define PG8_ROWS(_u) do { _Pragma("unroll") for (int _i = 0; _i < 2; ++_i) { voffA[_i] = S.row_off((_u), rselA[_i]) + cselA[_i]; voffA1[_i] = S.row_off((_u), HALF + rselA[_i]) + cselA[_i]; } } while (0)
; #define PG8_STAGE(bufoff, gbase, voff) do { _Pragma("unroll") for (int _i = 0; _i < 2; ++_i) \
;         __builtin_amdgcn_global_load_lds((const unsigned*)((const char*)(gbase) + (voff)[_i]), (PG8_LAS unsigned*)(lds + (bufoff) + ldsw + _i * 8192), 16, 0, 0); } while (0)
; #define PG8_WAIT_V(n) asm volatile("s_waitcnt vmcnt(" #n ")" ::: "memory")
; #define PG8_WAIT_L(n) asm volatile("s_waitcnt lgkmcnt(" #n ")" ::: "memory")
; #define PG8_BAR __builtin_amdgcn_s_barrier()
; #define PG8_SCHED __builtin_amdgcn_sched_barrier(0)
; template <class Epi, class Sched, bool ALIGN_EPI = false, bool SP2 = false, bool FP8 = false, bool I8 = false>
; __device__ __forceinline__ void gemm_phase(PG8_LAS unsigned char* lds, const Gemm g, const Sched& S, const Epi& E) {
;     ...
;             PG8_LDB(B0, 0, 0); PG8_LDB(B1, 0, 1); PG8_SCHED; PG8_LDA(At, 0, 0); PG8_STAGE(PG8_SA(1, 1), a1 + hstepA, voffA1);
;             PG8_WAIT_V(8); PG8_WAIT_L(0); PG8_BAR; PG8_MMA(0, 0, At, B0); PG8_MMA(0, 1, At, B1); PG8_BAR; PG8_SCHED;
;             if constexpr (Sched::GATHER) { if (last && has_next) PG8_ROWS(ui + 1); }
;             PG8_LDA(At, 0, 1); PG8_STAGE(PG8_SB(0, 0), b2, voffB); PG8_STAGE(PG8_SB(0, 1), b2 + hstep, voffB); PG8_STAGE(PG8_SA(0, 0), a2, voffA);
;             PG8_WAIT_V(8); PG8_WAIT_L(0); PG8_BAR; PG8_MMA(1, 0, At, B0); PG8_MMA(1, 1, At, B1); PG8_BAR; PG8_SCHED;
.LBB0_2397:
	ds_read_b128 v[16:19], v189
	ds_read_b128 v[20:23], v189 offset:1024
	ds_read_b128 v[24:27], v189 offset:2048
	ds_read_b128 v[28:31], v189 offset:3072
	ds_read_b128 v[0:3], v190
	ds_read_b128 v[4:7], v190 offset:1024
	ds_read_b128 v[8:11], v190 offset:2048
	ds_read_b128 v[12:15], v190 offset:3072
	s_add_u32 s28, s6, 0xfffc0080
	s_addc_u32 s29, s7, -1
	s_cmp_eq_u32 s52, 12
	s_cselect_b32 s31, s17, s29
	s_cselect_b32 s30, s19, s28
	s_cselect_b32 s29, s21, s51
	s_cselect_b32 s28, s20, s50
	v_lshl_add_u64 v[218:219], s[6:7], 0, v[172:173]
	s_add_i32 m0, s25, 0xc000
	ds_read_b128 v[176:179], v191
	ds_read_b128 v[180:183], v191 offset:1024
	ds_read_b128 v[194:197], v191 offset:2048
	ds_read_b128 v[198:201], v191 offset:3072
	ds_read_b128 v[202:205], v191 offset:4096
	ds_read_b128 v[206:209], v191 offset:5120
	ds_read_b128 v[210:213], v191 offset:6144
	ds_read_b128 v[214:217], v191 offset:7168
	global_load_lds_dwordx4 v[218:219], off
	v_lshl_add_u64 v[218:219], s[6:7], 0, v[174:175]
	s_add_i32 m0, s25, 0xe000
	s_nop 0
	global_load_lds_dwordx4 v[218:219], off
	s_waitcnt vmcnt(8)
	s_waitcnt lgkmcnt(0)
	s_barrier
	s_setprio 1
	s_waitcnt lgkmcnt(0)
	v_mfma_scale_f32_16x16x128_f8f6f4 v[156:159], v[16:23], v[176:183], v[156:159], v192, v192 op_sel_hi:[0,0,0]
	v_mfma_scale_f32_16x16x128_f8f6f4 v[152:155], v[24:31], v[176:183], v[152:155], v192, v192 op_sel_hi:[0,0,0]
	v_mfma_scale_f32_16x16x128_f8f6f4 v[148:151], v[16:23], v[194:201], v[148:151], v192, v192 op_sel_hi:[0,0,0]
	v_mfma_scale_f32_16x16x128_f8f6f4 v[144:147], v[24:31], v[194:201], v[144:147], v192, v192 op_sel_hi:[0,0,0]
	s_setprio 0
	s_setprio 1
	v_mfma_scale_f32_16x16x128_f8f6f4 v[140:143], v[16:23], v[202:209], v[140:143], v192, v192 op_sel_hi:[0,0,0]
	v_mfma_scale_f32_16x16x128_f8f6f4 v[136:139], v[24:31], v[202:209], v[136:139], v192, v192 op_sel_hi:[0,0,0]
	v_mfma_scale_f32_16x16x128_f8f6f4 v[132:135], v[16:23], v[210:217], v[132:135], v192, v192 op_sel_hi:[0,0,0]
	v_mfma_scale_f32_16x16x128_f8f6f4 v[128:131], v[24:31], v[210:217], v[128:131], v192, v192 op_sel_hi:[0,0,0]
	s_setprio 0
	s_setprio 1
	v_mfma_scale_f32_16x16x128_f8f6f4 v[104:107], v[0:7], v[176:183], v[104:107], v192, v192 op_sel_hi:[0,0,0]
	v_mfma_scale_f32_16x16x128_f8f6f4 v[92:95], v[8:15], v[176:183], v[92:95], v192, v192 op_sel_hi:[0,0,0]
	v_mfma_scale_f32_16x16x128_f8f6f4 v[88:91], v[0:7], v[194:201], v[88:91], v192, v192 op_sel_hi:[0,0,0]
	v_mfma_scale_f32_16x16x128_f8f6f4 v[80:83], v[8:15], v[194:201], v[80:83], v192, v192 op_sel_hi:[0,0,0]
	s_setprio 0
	s_setprio 1
	v_mfma_scale_f32_16x16x128_f8f6f4 v[76:79], v[0:7], v[202:209], v[76:79], v192, v192 op_sel_hi:[0,0,0]
	v_mfma_scale_f32_16x16x128_f8f6f4 v[72:75], v[8:15], v[202:209], v[72:75], v192, v192 op_sel_hi:[0,0,0]
	v_mfma_scale_f32_16x16x128_f8f6f4 v[68:71], v[0:7], v[210:217], v[68:71], v192, v192 op_sel_hi:[0,0,0]
	v_mfma_scale_f32_16x16x128_f8f6f4 v[64:67], v[8:15], v[210:217], v[64:67], v192, v192 op_sel_hi:[0,0,0]
	s_setprio 0
	s_barrier
	s_add_i32 s53, s43, s35
	v_lshl_add_u64 v[176:177], s[28:29], 0, v[168:169]
	s_mov_b32 m0, s53
	ds_read_b128 v[194:197], v191 offset:16384
	ds_read_b128 v[198:201], v191 offset:17408
	ds_read_b128 v[202:205], v191 offset:18432
	ds_read_b128 v[206:209], v191 offset:19456
	ds_read_b128 v[210:213], v191 offset:20480
	ds_read_b128 v[214:217], v191 offset:21504
	ds_read_b128 v[218:221], v191 offset:22528
	ds_read_b128 v[222:225], v191 offset:23552
	global_load_lds_dwordx4 v[176:177], off
	s_add_i32 m0, s53, 0x2000
	s_add_u32 s54, s28, 0x40000
	v_lshl_add_u64 v[178:179], s[28:29], 0, v[164:165]
	s_addc_u32 s55, s29, 0
	s_add_i32 s53, s44, s35
	global_load_lds_dwordx4 v[178:179], off
	v_lshl_add_u64 v[180:181], s[54:55], 0, v[168:169]
	s_mov_b32 m0, s53
	v_lshl_add_u64 v[182:183], s[30:31], 0, v[166:167]
	global_load_lds_dwordx4 v[180:181], off
	v_lshl_add_u64 v[180:181], s[54:55], 0, v[164:165]
	s_add_i32 m0, s53, 0x2000
	s_nop 0
	global_load_lds_dwordx4 v[180:181], off
	v_lshl_add_u64 v[180:181], s[30:31], 0, v[170:171]
	s_mov_b32 m0, s25
	s_nop 0
	global_load_lds_dwordx4 v[180:181], off
	s_mov_b32 m0, s27
	s_nop 0
	global_load_lds_dwordx4 v[182:183], off
	s_waitcnt vmcnt(8)
	s_waitcnt lgkmcnt(0)
	s_barrier
	s_setprio 1
	s_waitcnt lgkmcnt(0)
	v_mfma_scale_f32_16x16x128_f8f6f4 v[124:127], v[16:23], v[194:201], v[124:127], v192, v192 op_sel_hi:[0,0,0]
	v_mfma_scale_f32_16x16x128_f8f6f4 v[120:123], v[24:31], v[194:201], v[120:123], v192, v192 op_sel_hi:[0,0,0]
	v_mfma_scale_f32_16x16x128_f8f6f4 v[116:119], v[16:23], v[202:209], v[116:119], v192, v192 op_sel_hi:[0,0,0]
	v_mfma_scale_f32_16x16x128_f8f6f4 v[112:115], v[24:31], v[202:209], v[112:115], v192, v192 op_sel_hi:[0,0,0]
	s_setprio 0
	s_setprio 1
	v_mfma_scale_f32_16x16x128_f8f6f4 v[108:111], v[16:23], v[210:217], v[108:111], v192, v192 op_sel_hi:[0,0,0]
	v_mfma_scale_f32_16x16x128_f8f6f4 v[100:103], v[24:31], v[210:217], v[100:103], v192, v192 op_sel_hi:[0,0,0]
	v_mfma_scale_f32_16x16x128_f8f6f4 v[96:99], v[16:23], v[218:225], v[96:99], v192, v192 op_sel_hi:[0,0,0]
	v_mfma_scale_f32_16x16x128_f8f6f4 v[84:87], v[24:31], v[218:225], v[84:87], v192, v192 op_sel_hi:[0,0,0]
	s_setprio 0
	s_setprio 1
	v_mfma_scale_f32_16x16x128_f8f6f4 v[60:63], v[0:7], v[194:201], v[60:63], v192, v192 op_sel_hi:[0,0,0]
	v_mfma_scale_f32_16x16x128_f8f6f4 v[56:59], v[8:15], v[194:201], v[56:59], v192, v192 op_sel_hi:[0,0,0]
	v_mfma_scale_f32_16x16x128_f8f6f4 v[52:55], v[0:7], v[202:209], v[52:55], v192, v192 op_sel_hi:[0,0,0]
	v_mfma_scale_f32_16x16x128_f8f6f4 v[48:51], v[8:15], v[202:209], v[48:51], v192, v192 op_sel_hi:[0,0,0]
	s_setprio 0
	s_setprio 1
	v_mfma_scale_f32_16x16x128_f8f6f4 v[44:47], v[0:7], v[210:217], v[44:47], v192, v192 op_sel_hi:[0,0,0]
	v_mfma_scale_f32_16x16x128_f8f6f4 v[40:43], v[8:15], v[210:217], v[40:43], v192, v192 op_sel_hi:[0,0,0]
	v_mfma_scale_f32_16x16x128_f8f6f4 v[36:39], v[0:7], v[218:225], v[36:39], v192, v192 op_sel_hi:[0,0,0]
	v_mfma_scale_f32_16x16x128_f8f6f4 v[32:35], v[8:15], v[218:225], v[32:35], v192, v192 op_sel_hi:[0,0,0]
	s_setprio 0
	s_barrier
; #define PG8_STAGE(bufoff, gbase, voff) do { _Pragma("unroll") for (int _i = 0; _i < 2; ++_i) \
;         __builtin_amdgcn_global_load_lds((const unsigned*)((const char*)(gbase) + (voff)[_i]), (PG8_LAS unsigned*)(lds + (bufoff) + ldsw + _i * 8192), 16, 0, 0); } while (0)
; #define PG8_WAIT_V(n) asm volatile("s_waitcnt vmcnt(" #n ")" ::: "memory")
; #define PG8_WAIT_L(n) asm volatile("s_waitcnt lgkmcnt(" #n ")" ::: "memory")
; #define PG8_BAR __builtin_amdgcn_s_barrier()
; #define PG8_SCHED __builtin_amdgcn_sched_barrier(0)
; template <class Epi, class Sched, bool ALIGN_EPI = false, bool SP2 = false, bool FP8 = false, bool I8 = false>
; __device__ __forceinline__ void gemm_phase(PG8_LAS unsigned char* lds, const Gemm g, const Sched& S, const Epi& E) {
;     ...
;             PG8_LDB(B0, 1, 0); PG8_LDB(B1, 1, 1); PG8_SCHED; PG8_LDA(At, 1, 0); PG8_STAGE(PG8_SA(0, 1), a2 + hstepA, voffA1);
;             PG8_WAIT_V(8); PG8_WAIT_L(0); PG8_BAR; PG8_MMA(0, 0, At, B0); PG8_MMA(0, 1, At, B1); PG8_BAR; PG8_SCHED;
;             PG8_LDA(At, 1, 1); PG8_STAGE(PG8_SB(1, 0), b3, voffB); PG8_STAGE(PG8_SB(1, 1), b3 + hstep, voffB); PG8_STAGE(PG8_SA(1, 0), a3, voffA);
;             PG8_WAIT_V(8); PG8_WAIT_L(0); PG8_BAR; PG8_MMA(1, 0, At, B0); PG8_MMA(1, 1, At, B1); PG8_BAR; PG8_SCHED;
	s_add_i32 s53, 0, 0x18000
	s_add_i32 s54, 0, 0x1c000
	v_add_u32_e32 v12, s53, v163
	v_add_u32_e32 v28, s54, v163
	ds_read_b128 v[0:3], v12
	ds_read_b128 v[4:7], v12 offset:1024
	ds_read_b128 v[8:11], v12 offset:2048
	ds_read_b128 v[12:15], v12 offset:3072
	ds_read_b128 v[16:19], v28
	ds_read_b128 v[20:23], v28 offset:1024
	ds_read_b128 v[24:27], v28 offset:2048
	ds_read_b128 v[28:31], v28 offset:3072
	s_add_u32 s30, s30, 0x40000
	s_addc_u32 s31, s31, 0
	s_mov_b32 m0, s39
	v_lshl_add_u64 v[226:227], s[30:31], 0, v[170:171]
	ds_read_b128 v[194:197], v191 offset:32768
	ds_read_b128 v[198:201], v191 offset:33792
	ds_read_b128 v[202:205], v191 offset:34816
	ds_read_b128 v[206:209], v191 offset:35840
	ds_read_b128 v[210:213], v191 offset:36864
	ds_read_b128 v[214:217], v191 offset:37888
	ds_read_b128 v[218:221], v191 offset:38912
	ds_read_b128 v[222:225], v191 offset:39936
	global_load_lds_dwordx4 v[226:227], off
	v_lshl_add_u64 v[226:227], s[30:31], 0, v[166:167]
	s_mov_b32 m0, s40
	s_nop 0
	global_load_lds_dwordx4 v[226:227], off
	s_waitcnt vmcnt(8)
	s_waitcnt lgkmcnt(0)
	s_barrier
	s_setprio 1
	s_waitcnt lgkmcnt(0)
	v_mfma_scale_f32_16x16x128_f8f6f4 v[156:159], v[0:7], v[194:201], v[156:159], v192, v192 op_sel_hi:[0,0,0]
	v_mfma_scale_f32_16x16x128_f8f6f4 v[152:155], v[8:15], v[194:201], v[152:155], v192, v192 op_sel_hi:[0,0,0]
	v_mfma_scale_f32_16x16x128_f8f6f4 v[148:151], v[0:7], v[202:209], v[148:151], v192, v192 op_sel_hi:[0,0,0]
	v_mfma_scale_f32_16x16x128_f8f6f4 v[144:147], v[8:15], v[202:209], v[144:147], v192, v192 op_sel_hi:[0,0,0]
	s_setprio 0
	s_setprio 1
	v_mfma_scale_f32_16x16x128_f8f6f4 v[140:143], v[0:7], v[210:217], v[140:143], v192, v192 op_sel_hi:[0,0,0]
	v_mfma_scale_f32_16x16x128_f8f6f4 v[136:139], v[8:15], v[210:217], v[136:139], v192, v192 op_sel_hi:[0,0,0]
	v_mfma_scale_f32_16x16x128_f8f6f4 v[132:135], v[0:7], v[218:225], v[132:135], v192, v192 op_sel_hi:[0,0,0]
	v_mfma_scale_f32_16x16x128_f8f6f4 v[128:131], v[8:15], v[218:225], v[128:131], v192, v192 op_sel_hi:[0,0,0]
	s_setprio 0
	s_setprio 1
	v_mfma_scale_f32_16x16x128_f8f6f4 v[104:107], v[16:23], v[194:201], v[104:107], v192, v192 op_sel_hi:[0,0,0]
	v_mfma_scale_f32_16x16x128_f8f6f4 v[92:95], v[24:31], v[194:201], v[92:95], v192, v192 op_sel_hi:[0,0,0]
	v_mfma_scale_f32_16x16x128_f8f6f4 v[88:91], v[16:23], v[202:209], v[88:91], v192, v192 op_sel_hi:[0,0,0]
	v_mfma_scale_f32_16x16x128_f8f6f4 v[80:83], v[24:31], v[202:209], v[80:83], v192, v192 op_sel_hi:[0,0,0]
	s_setprio 0
	s_setprio 1
	v_mfma_scale_f32_16x16x128_f8f6f4 v[76:79], v[16:23], v[210:217], v[76:79], v192, v192 op_sel_hi:[0,0,0]
	v_mfma_scale_f32_16x16x128_f8f6f4 v[72:75], v[24:31], v[210:217], v[72:75], v192, v192 op_sel_hi:[0,0,0]
	v_mfma_scale_f32_16x16x128_f8f6f4 v[68:71], v[16:23], v[218:225], v[68:71], v192, v192 op_sel_hi:[0,0,0]
	v_mfma_scale_f32_16x16x128_f8f6f4 v[64:67], v[24:31], v[218:225], v[64:67], v192, v192 op_sel_hi:[0,0,0]
	s_setprio 0
	s_barrier
	s_add_i32 s30, s53, s35
	v_lshl_add_u64 v[176:177], v[176:177], 0, s[10:11]
	s_mov_b32 m0, s30
	ds_read_b128 v[194:197], v191 offset:49152
	ds_read_b128 v[198:201], v191 offset:50176
	ds_read_b128 v[202:205], v191 offset:51200
	ds_read_b128 v[206:209], v191 offset:52224
	ds_read_b128 v[210:213], v191 offset:53248
	ds_read_b128 v[214:217], v191 offset:54272
	ds_read_b128 v[218:221], v191 offset:55296
	ds_read_b128 v[222:225], v191 offset:56320
	global_load_lds_dwordx4 v[176:177], off
	s_add_i32 m0, s30, 0x2000
	s_add_u32 s28, s28, 0x40080
	v_lshl_add_u64 v[176:177], v[178:179], 0, s[10:11]
	s_addc_u32 s29, s29, 0
	s_add_i32 s30, s54, s35
	global_load_lds_dwordx4 v[176:177], off
	v_lshl_add_u64 v[176:177], s[28:29], 0, v[168:169]
	s_mov_b32 m0, s30
	s_nop 0
	global_load_lds_dwordx4 v[176:177], off
	v_lshl_add_u64 v[176:177], s[28:29], 0, v[164:165]
	s_add_i32 m0, s30, 0x2000
	s_nop 0
	global_load_lds_dwordx4 v[176:177], off
	v_lshl_add_u64 v[176:177], v[180:181], 0, s[10:11]
	s_mov_b32 m0, s41
	s_nop 0
	global_load_lds_dwordx4 v[176:177], off
	v_lshl_add_u64 v[176:177], v[182:183], 0, s[10:11]
	s_mov_b32 m0, s42
	s_nop 0
	global_load_lds_dwordx4 v[176:177], off
	s_waitcnt vmcnt(8)
	s_waitcnt lgkmcnt(0)
	s_barrier
	s_setprio 1
	s_waitcnt lgkmcnt(0)
	v_mfma_scale_f32_16x16x128_f8f6f4 v[124:127], v[0:7], v[194:201], v[124:127], v192, v192 op_sel_hi:[0,0,0]
	v_mfma_scale_f32_16x16x128_f8f6f4 v[120:123], v[8:15], v[194:201], v[120:123], v192, v192 op_sel_hi:[0,0,0]
	v_mfma_scale_f32_16x16x128_f8f6f4 v[116:119], v[0:7], v[202:209], v[116:119], v192, v192 op_sel_hi:[0,0,0]
	v_mfma_scale_f32_16x16x128_f8f6f4 v[112:115], v[8:15], v[202:209], v[112:115], v192, v192 op_sel_hi:[0,0,0]
	s_setprio 0
	s_setprio 1
	v_mfma_scale_f32_16x16x128_f8f6f4 v[108:111], v[0:7], v[210:217], v[108:111], v192, v192 op_sel_hi:[0,0,0]
	v_mfma_scale_f32_16x16x128_f8f6f4 v[100:103], v[8:15], v[210:217], v[100:103], v192, v192 op_sel_hi:[0,0,0]
	v_mfma_scale_f32_16x16x128_f8f6f4 v[96:99], v[0:7], v[218:225], v[96:99], v192, v192 op_sel_hi:[0,0,0]
	v_mfma_scale_f32_16x16x128_f8f6f4 v[84:87], v[8:15], v[218:225], v[84:87], v192, v192 op_sel_hi:[0,0,0]
	s_setprio 0
	s_setprio 1
	v_mfma_scale_f32_16x16x128_f8f6f4 v[60:63], v[16:23], v[194:201], v[60:63], v192, v192 op_sel_hi:[0,0,0]
	v_mfma_scale_f32_16x16x128_f8f6f4 v[56:59], v[24:31], v[194:201], v[56:59], v192, v192 op_sel_hi:[0,0,0]
	v_mfma_scale_f32_16x16x128_f8f6f4 v[52:55], v[16:23], v[202:209], v[52:55], v192, v192 op_sel_hi:[0,0,0]
	v_mfma_scale_f32_16x16x128_f8f6f4 v[48:51], v[24:31], v[202:209], v[48:51], v192, v192 op_sel_hi:[0,0,0]
	s_setprio 0
	s_setprio 1
	v_mfma_scale_f32_16x16x128_f8f6f4 v[44:47], v[16:23], v[210:217], v[44:47], v192, v192 op_sel_hi:[0,0,0]
	v_mfma_scale_f32_16x16x128_f8f6f4 v[40:43], v[24:31], v[210:217], v[40:43], v192, v192 op_sel_hi:[0,0,0]
	v_mfma_scale_f32_16x16x128_f8f6f4 v[36:39], v[16:23], v[218:225], v[36:39], v192, v192 op_sel_hi:[0,0,0]
	v_mfma_scale_f32_16x16x128_f8f6f4 v[32:35], v[24:31], v[218:225], v[32:35], v192, v192 op_sel_hi:[0,0,0]
	s_setprio 0
	s_barrier
	s_add_i32 s52, s52, 2
	s_add_u32 s6, s6, 0x100
	s_addc_u32 s7, s7, 0
	s_add_u32 s50, s50, 0x100
	s_addc_u32 s51, s51, 0
	s_cmp_gt_u32 s52, 13
	s_cbranch_scc0 .LBB0_2397
	s_and_b64 vcc, exec, s[12:13]
	s_cbranch_vccz .LBB0_2400
	s_barrier
